# pool2 epilogue de-serialised: the four LDS reads of the other half's partial tile issued together, store ladder uses immediate offsets off one address register
# baseline (speedup 1.0000x reference)
.LBB4_37:
	s_or_b64 exec, exec, s[4:5]
	s_waitcnt lgkmcnt(0)
	s_barrier
	s_and_saveexec_b64 s[0:1], vcc
	s_cbranch_execz .LBB4_39
	v_lshl_or_b32 v0, v93, 12, v0
	ds_read_b128 v[18:21], v0 offset:33792
	ds_read_b128 v[22:25], v0 offset:34816
	ds_read_b128 v[30:33], v0 offset:35840
	ds_read_b128 v[34:37], v0 offset:36864
	s_mov_b32 s3, 0
	s_lshl_b64 s[0:1], s[2:3], 15
	v_or_b32_e32 v26, v91, v90
	v_lshlrev_b32_e32 v27, 7, v66
	v_lshlrev_b32_e32 v1, 9, v1
	s_add_u32 s0, s12, s0
	v_or3_b32 v1, v1, v27, v26
	s_addc_u32 s1, s13, s1
	v_lshlrev_b32_e32 v1, 2, v1
	s_waitcnt lgkmcnt(3)
	v_add_f32_e32 v14, v14, v18
	v_add_f32_e32 v15, v15, v19
	v_add_f32_e32 v16, v16, v20
	v_add_f32_e32 v17, v17, v21
	global_store_dword v1, v14, s[0:1]
	global_store_dword v1, v15, s[0:1] offset:512
	global_store_dword v1, v16, s[0:1] offset:1024
	global_store_dword v1, v17, s[0:1] offset:1536
	s_waitcnt lgkmcnt(2)
	v_add_f32_e32 v10, v10, v22
	v_add_f32_e32 v11, v11, v23
	v_add_f32_e32 v12, v12, v24
	v_add_f32_e32 v13, v13, v25
	global_store_dword v1, v10, s[0:1] offset:64
	global_store_dword v1, v11, s[0:1] offset:576
	global_store_dword v1, v12, s[0:1] offset:1088
	global_store_dword v1, v13, s[0:1] offset:1600
	s_waitcnt lgkmcnt(1)
	v_add_f32_e32 v6, v6, v30
	v_add_f32_e32 v7, v7, v31
	v_add_f32_e32 v8, v8, v32
	v_add_f32_e32 v9, v9, v33
	global_store_dword v1, v6, s[0:1] offset:128
	global_store_dword v1, v7, s[0:1] offset:640
	global_store_dword v1, v8, s[0:1] offset:1152
	global_store_dword v1, v9, s[0:1] offset:1664
	s_waitcnt lgkmcnt(0)
	v_add_f32_e32 v2, v2, v34
	v_add_f32_e32 v3, v3, v35
	v_add_f32_e32 v4, v4, v36
	v_add_f32_e32 v5, v5, v37
	global_store_dword v1, v2, s[0:1] offset:192
	global_store_dword v1, v3, s[0:1] offset:704
	global_store_dword v1, v4, s[0:1] offset:1216
	global_store_dword v1, v5, s[0:1] offset:1728
